# v032 + 8.8% of the MoE weight conversion (last 5952 items, layer-1 experts 13-15) moved out of the prologue into the 248 workgroups that idle during the ctx out-projection call of phase 4
# speedup vs baseline: 1.0058x; 1.0058x over previous
; #define LAS __attribute__((address_space(3)))
; __device__ __forceinline__ int tidx() { int t = threadIdx.x; asm volatile("" : "+v"(t)); return t; }
; __device__ __forceinline__ void cvt_item(const float* W, int K, int N, bf16_t* WT, int drow0, int k0, int n0, LAS float* scr, int lane) {
;     f32x4 v[16];
;     const int lr = lane >> 4, lc4 = (lane & 15) * 4;
; #pragma unroll
; __device__ __forceinline__ void phase_cvt_moe(LAS unsigned char* lds, const CvtMoe a) {
;     const int tid_ = tidx(), wave = tid_ >> 6, lane = tid_ & 63;
;     LAS float* scr = (LAS float*)(lds + wave * CVT_SCR);
;     const int gw = blockIdx.x * 8 + wave, NGW = gridDim.x * 8;
;     constexpr int IG = (D / 64) * (FF / 64), ID = (FF / 64) * (D / 64);
;     for (int it = gw; it < 2 * NE * (2 * IG + ID); it += NGW) {
;         const int e = it / (2 * IG + ID); int r = it % (2 * IG + ID);
;         if (r < 2 * IG) { const int up = r / IG; r %= IG; const int nblk = FF / 64, kb = r / nblk, nb = r % nblk, n0 = nb * 64;
;             cvt_item((up ? a.wu : a.wg) + (size_t)e * D * FF, D, FF, a.gu + (size_t)e * 2 * FF * D, (n0 / 128) * 256 + up * 128 + (n0 % 128), kb * 64, n0, scr, lane); }
;         else { r -= 2 * IG; const int nblk = D / 64, kb = r / nblk, nb = r % nblk; cvt_item(a.wd + (size_t)e * FF * D, FF, D, a.dn + (size_t)e * D * FF, nb * 64, kb * 64, nb * 64, scr, lane); }
;     }
.LBB0_55:
	s_or_b64 exec, exec, s[4:5]
	s_add_u32 s4, s90, 0x30a13600
	s_addc_u32 s5, s91, 0
	v_writelane_b32 v250, s4, 6
	v_mov_b32_e32 v4, v0
	s_nop 0
	v_writelane_b32 v250, s5, 7
	s_add_u32 s4, s90, 0x46a13600
	s_addc_u32 s5, s91, 0
	v_writelane_b32 v250, s4, 8
	v_ashrrev_i32_e32 v2, 6, v4
	v_add_u32_e32 v5, s14, v2
	v_writelane_b32 v250, s5, 9
	s_mov_b32 s4, 0xf0c0
	v_cmp_gt_i32_e32 vcc, s4, v5
	s_and_saveexec_b64 s[4:5], vcc
	s_cbranch_execz .LBB0_62
	s_movk_i32 s6, 0x4100
	v_mul_lo_u32 v3, v2, s6
	v_add_u32_e32 v8, 0, v3
	v_lshlrev_b32_e32 v3, 2, v4
	v_bfe_u32 v6, v4, 4, 2
	v_and_b32_e32 v44, 60, v3
	v_bfe_u32 v7, v4, 3, 3
	v_lshlrev_b32_e32 v4, 3, v4
	v_lshl_add_u32 v20, v44, 2, v8
	v_mul_u32_u24_e32 v21, 0x104, v6
	v_and_b32_e32 v4, 56, v4
	v_mul_u32_u24_e32 v9, 0x104, v4
	v_lshlrev_b32_e32 v10, 2, v7
	v_lshlrev_b32_e32 v16, 2, v2
	v_add_u32_e32 v20, v20, v21
	v_mov_b32_e32 v3, 0
	v_add3_u32 v8, v8, v9, v10
	v_or_b32_e32 v9, 8, v7
	v_or_b32_e32 v10, 16, v7
	v_or_b32_e32 v11, 24, v7
	v_or_b32_e32 v12, 32, v7
	v_or_b32_e32 v13, 40, v7
	v_or_b32_e32 v14, 48, v7
	v_or_b32_e32 v15, 56, v7
	v_lshl_add_u32 v16, s2, 5, v16
	v_lshlrev_b32_e32 v17, 2, v1
	v_lshl_add_u32 v18, v2, 6, s3
	v_lshlrev_b32_e32 v19, 6, v1
	s_mov_b64 s[6:7], 0
	s_mov_b32 s3, 0x3e0f83e1
	s_movk_i32 s10, 0x57f
	s_mov_b32 s11, 0xb00000
	v_add_u32_e32 v21, 0x410, v20
	v_add_u32_e32 v22, 0x418, v20
	v_add_u32_e32 v23, 0x820, v20
	v_add_u32_e32 v24, 0x828, v20
	v_add_u32_e32 v25, 0xc30, v20
	v_add_u32_e32 v26, 0xc38, v20
	v_add_u32_e32 v27, 0x1040, v20
	v_add_u32_e32 v28, 0x1048, v20
	v_add_u32_e32 v29, 0x1450, v20
	v_add_u32_e32 v30, 0x1458, v20
	v_add_u32_e32 v31, 0x1860, v20
	v_add_u32_e32 v32, 0x1868, v20
	v_add_u32_e32 v33, 0x1c70, v20
	v_add_u32_e32 v34, 0x1c78, v20
	v_add_u32_e32 v35, 0x2080, v20
	v_add_u32_e32 v36, 0x2088, v20
	v_add_u32_e32 v37, 0x2490, v20
	v_add_u32_e32 v38, 0x2498, v20
	v_add_u32_e32 v39, 0x28a0, v20
	v_add_u32_e32 v40, 0x28a8, v20
	v_add_u32_e32 v41, 0x2cb0, v20
	v_add_u32_e32 v42, 0x2cb8, v20
	s_movk_i32 s12, 0xba3
	s_mov_b32 s13, 0xb000
	s_mov_b32 s14, 0x16000
	s_mov_b32 s15, 0x21000
	s_mov_b32 s16, 0x2c000
	s_mov_b32 s17, 0x37000
	s_mov_b32 s18, 0x42000
	s_mov_b32 s19, 0x4d000
	s_mov_b32 s20, 0x58000
	s_mov_b32 s21, 0x63000
	s_mov_b32 s22, 0x6e000
	s_mov_b32 s23, 0x79000
	s_mov_b32 s24, 0x84000
	s_mov_b32 s25, 0x8f000
	s_mov_b32 s26, 0x9a000
	s_mov_b32 s27, 0xa5000
	s_mov_b32 s28, 0xf0bf
	v_lshlrev_b32_e32 v2, 2, v44
	v_add_u32_e32 v43, 0x30c0, v20
	v_add_u32_e32 v44, 0x30c8, v20
	v_add_u32_e32 v45, 0x34d0, v20
	v_add_u32_e32 v46, 0x34d8, v20
	v_mov_b32_e32 v47, 6
	v_mov_b32_e32 v48, 1
	v_mov_b32_e32 v49, 8
	v_mov_b32_e32 v50, 7
	s_branch .LBB0_58

; #define LAS __attribute__((address_space(3)))
; __device__ __forceinline__ int tidx() { int t = threadIdx.x; asm volatile("" : "+v"(t)); return t; }
; __device__ __forceinline__ u32x4 pack8(const f32x4 a, const f32x4 b) { u32x4 w; w.x = cvt_pk_bf16(a[0], a[1]); w.y = cvt_pk_bf16(a[2], a[3]); w.z = cvt_pk_bf16(b[0], b[1]); w.w = cvt_pk_bf16(b[2], b[3]); return w; }
; __device__ __forceinline__ void phase_cvt_moe(LAS unsigned char* lds, const CvtMoe a) {
;     const int tid_ = tidx(), wave = tid_ >> 6, lane = tid_ & 63;
;     LAS float* scr = (LAS float*)(lds + wave * CVT_SCR);
;     const int gw = blockIdx.x * 8 + wave, NGW = gridDim.x * 8;
;     constexpr int IG = (D / 64) * (FF / 64), ID = (FF / 64) * (D / 64);
;     for (int it = gw; it < 2 * NE * (2 * IG + ID); it += NGW) {
;         const int e = it / (2 * IG + ID); int r = it % (2 * IG + ID);
;         if (r < 2 * IG) { const int up = r / IG; r %= IG; const int nblk = FF / 64, kb = r / nblk, nb = r % nblk, n0 = nb * 64;
;     __device__ __forceinline__ void fused(f32x4 (&acc)[2][2][4][2], const pg8::Unit& u_, int wr_, int wc_, int fr_, int fq_, LAS unsigned char* lds, int tid_) const {
;     ...
;         for (int bj = 0; bj < 2; ++bj) { f32x4 G[2], SH[2];
; #pragma unroll
;             for (int n = 0; n < 2; ++n) { const int c = col0 + bj * HALF + 4 * n; const f32x4 gg = *(const f32x4*)(g2 + c), sc = *(const f32x4*)(mrow + 4 * D + c);
;                 G[n] = gg * (sc + 1.f); SH[n] = *(const f32x4*)(mrow + 3 * D + c); }
; #pragma unroll
;             for (int ai = 0; ai < 2; ++ai)
; #pragma unroll
;                 for (int m = 0; m < 4; ++m) { const int rl = ai * HALF + wr * 64 + m * 16 + fr; const float r = bad ? __builtin_nanf("") : Sr[rl];
;                     *(u32x4*)(HB + (size_t)(u.pm * BM + rl) * D + col0 + bj * HALF) = pack8(acc[ai][bj][m][0] * r * G[0] + SH[0], acc[ai][bj][m][1] * r * G[1] + SH[1]); }
;             asm volatile("" ::: "memory"); }
.LBB0_639:
	s_waitcnt lgkmcnt(0)
	v_pk_mul_f32 v[16:17], v[14:15], v[136:137] op_sel_hi:[0,1]
	v_pk_mul_f32 v[22:23], v[14:15], v[134:135] op_sel_hi:[0,1]
	v_pk_fma_f32 v[8:9], v[20:21], v[16:17], v[8:9]
	v_pk_mul_f32 v[16:17], v[14:15], v[132:133] op_sel_hi:[0,1]
	v_pk_mul_f32 v[14:15], v[14:15], v[130:131] op_sel_hi:[0,1]
	v_pk_fma_f32 v[6:7], v[18:19], v[22:23], v[6:7]
	v_pk_fma_f32 v[12:13], v[12:13], v[16:17], v[4:5]
	v_pk_fma_f32 v[4:5], v[10:11], v[14:15], v[2:3]
	v_cvt_pk_bf16_f32 v2, v6, v7
	v_cvt_pk_bf16_f32 v3, v8, v9
	v_cvt_pk_bf16_f32 v4, v4, v5
	v_cvt_pk_bf16_f32 v5, v12, v13
	global_store_dwordx4 v[72:73], v[2:5], off offset:256
	s_andn2_b64 vcc, exec, s[30:31]
	s_mov_b64 s[0:1], -1
	s_cbranch_vccnz .LBB0_553
	v_readlane_b32 s0, v250, 32
	v_readlane_b32 s1, v250, 33
	s_andn2_b64 vcc, exec, s[0:1]
	s_cbranch_vccnz .LBB0_552
	s_barrier
	s_branch .LBB0_552
	s_branch .LBB0_642
.Lcvp4b_entry:
	s_sub_i32 s0, s94, 8
	v_readlane_b32 s2, v250, 26
	v_readlane_b32 s3, v250, 27
	s_nop 3
	s_sub_u32 s2, s2, 0xc0
	s_subb_u32 s3, s3, 0
	s_load_dwordx2 s[38:39], s[2:3], 0x90
	s_load_dwordx2 s[40:41], s[2:3], 0x98
	s_load_dwordx2 s[48:49], s[2:3], 0xa0
	s_lshl_b32 s0, s0, 3
	s_add_i32 s0, s0, 0xf0c0
	v_mov_b32_e32 v131, 0x7c0
	s_waitcnt lgkmcnt(0)
	s_add_u32 s4, s90, 0x30a13600
	s_addc_u32 s5, s91, 0
	v_writelane_b32 v250, s4, 6
	v_mov_b32_e32 v130, v0
	s_nop 0
	v_writelane_b32 v250, s5, 7
	s_add_u32 s4, s90, 0x46a13600
	s_addc_u32 s5, s91, 0
	v_writelane_b32 v250, s4, 8
	v_ashrrev_i32_e32 v2, 6, v130
	v_add_u32_e32 v5, s0, v2
	v_writelane_b32 v250, s5, 9
	s_mov_b32 s4, 0x10800
	v_cmp_gt_i32_e32 vcc, s4, v5
	s_and_saveexec_b64 s[4:5], vcc
	s_cbranch_execz .Lcvp4b_62
	s_movk_i32 s6, 0x4100
	v_mul_lo_u32 v3, v2, s6
	v_add_u32_e32 v8, 0, v3
	v_lshlrev_b32_e32 v3, 2, v130
	v_bfe_u32 v6, v130, 4, 2
	v_and_b32_e32 v44, 60, v3
	v_bfe_u32 v7, v130, 3, 3
	v_lshlrev_b32_e32 v130, 3, v130
	v_lshl_add_u32 v20, v44, 2, v8
	v_mul_u32_u24_e32 v21, 0x104, v6
	v_and_b32_e32 v130, 56, v130
	v_mul_u32_u24_e32 v9, 0x104, v130
	v_lshlrev_b32_e32 v10, 2, v7
	v_lshlrev_b32_e32 v16, 2, v2
	v_add_u32_e32 v20, v20, v21
	v_mov_b32_e32 v3, 0
	v_add3_u32 v8, v8, v9, v10
	v_or_b32_e32 v9, 8, v7
	v_or_b32_e32 v10, 16, v7
	v_or_b32_e32 v11, 24, v7
	v_or_b32_e32 v12, 32, v7
	v_or_b32_e32 v13, 40, v7
	v_or_b32_e32 v14, 48, v7
	v_or_b32_e32 v15, 56, v7
	v_lshlrev_b32_e32 v16, 2, v5
	v_lshlrev_b32_e32 v17, 2, v131
	v_lshlrev_b32_e32 v18, 6, v5
	v_lshlrev_b32_e32 v19, 6, v131
	s_mov_b64 s[6:7], 0
	s_mov_b32 s3, 0x3e0f83e1
	s_movk_i32 s10, 0x57f
	s_mov_b32 s11, 0xb00000
	v_add_u32_e32 v21, 0x410, v20
	v_add_u32_e32 v22, 0x418, v20
	v_add_u32_e32 v23, 0x820, v20
	v_add_u32_e32 v24, 0x828, v20
	v_add_u32_e32 v25, 0xc30, v20
	v_add_u32_e32 v26, 0xc38, v20
	v_add_u32_e32 v27, 0x1040, v20
	v_add_u32_e32 v28, 0x1048, v20
	v_add_u32_e32 v29, 0x1450, v20
	v_add_u32_e32 v30, 0x1458, v20
	v_add_u32_e32 v31, 0x1860, v20
	v_add_u32_e32 v32, 0x1868, v20
	v_add_u32_e32 v33, 0x1c70, v20
	v_add_u32_e32 v34, 0x1c78, v20
	v_add_u32_e32 v35, 0x2080, v20
	v_add_u32_e32 v36, 0x2088, v20
	v_add_u32_e32 v37, 0x2490, v20
	v_add_u32_e32 v38, 0x2498, v20
	v_add_u32_e32 v39, 0x28a0, v20
	v_add_u32_e32 v40, 0x28a8, v20
	v_add_u32_e32 v41, 0x2cb0, v20
	v_add_u32_e32 v42, 0x2cb8, v20
	s_movk_i32 s64, 0xba3
	s_mov_b32 s65, 0xb000
	s_mov_b32 s66, 0x16000
	s_mov_b32 s67, 0x21000
	s_mov_b32 s16, 0x2c000
	s_mov_b32 s68, 0x37000
	s_mov_b32 s69, 0x42000
	s_mov_b32 s19, 0x4d000
	s_mov_b32 s20, 0x58000
	s_mov_b32 s21, 0x63000
	s_mov_b32 s70, 0x6e000
	s_mov_b32 s23, 0x79000
	s_mov_b32 s24, 0x84000
	s_mov_b32 s25, 0x8f000
	s_mov_b32 s26, 0x9a000
	s_mov_b32 s27, 0xa5000
	s_mov_b32 s71, 0x107ff
	v_lshlrev_b32_e32 v2, 2, v44
	v_add_u32_e32 v43, 0x30c0, v20
	v_add_u32_e32 v44, 0x30c8, v20
	v_add_u32_e32 v45, 0x34d0, v20
	v_add_u32_e32 v46, 0x34d8, v20
	v_mov_b32_e32 v47, 6
	v_mov_b32_e32 v132, 1
	v_mov_b32_e32 v133, 8
	v_mov_b32_e32 v134, 7
	s_branch .Lcvp4b_58
.Lcvp4b_57:
	s_or_b64 exec, exec, s[8:9]
	v_add_u32_e32 v5, v5, v131
	v_cmp_lt_i32_e32 vcc, s71, v5
	v_add_u32_e32 v16, v16, v17
	s_or_b64 s[6:7], vcc, s[6:7]
	v_add_u32_e32 v18, v18, v19
	s_andn2_b64 exec, exec, s[6:7]
	s_cbranch_execz .Lcvp4b_62
.Lcvp4b_58:
	v_mul_hi_i32 v135, v5, s3
	v_lshrrev_b32_e32 v136, 31, v135
	v_ashrrev_i32_e32 v135, 9, v135
	v_add_u32_e32 v135, v135, v136
	v_mul_i32_i24_e32 v137, 0x840, v135
	v_sub_u32_e32 v136, v5, v137
	v_cmp_lt_i32_e32 vcc, s10, v136
	s_and_saveexec_b64 s[8:9], vcc
	s_xor_b64 s[8:9], exec, s[8:9]
	s_cbranch_execz .Lcvp4b_60
; #define LAS __attribute__((address_space(3)))
; __device__ __forceinline__ void cvt_item(const float* W, int K, int N, bf16_t* WT, int drow0, int k0, int n0, LAS float* scr, int lane) {
;     f32x4 v[16];
;     const int lr = lane >> 4, lc4 = (lane & 15) * 4;
; #pragma unroll
;     for (int i = 0; i < 16; ++i) v[i] = __builtin_nontemporal_load((const f32x4*)(W + (size_t)(k0 + 4 * i + lr) * N + n0 + lc4));
; #pragma unroll
;     for (int i = 0; i < 16; ++i) { LAS float* d = scr + (4 * i + lr) * 65 + lc4; d[0] = v[i][0]; d[1] = v[i][1]; d[2] = v[i][2]; d[3] = v[i][3]; }
; __device__ __forceinline__ void phase_cvt_moe(LAS unsigned char* lds, const CvtMoe a) {
;     ...
;         else { r -= 2 * IG; const int nblk = D / 64, kb = r / nblk, nb = r % nblk; cvt_item(a.wd + (size_t)e * FF * D, FF, D, a.dn + (size_t)e * D * FF, nb * 64, kb * 64, nb * 64, scr, lane); }
	v_lshlrev_b32_e32 v136, 6, v137
	v_sub_u32_e32 v118, v18, v136
	v_lshlrev_b32_e32 v136, 2, v137
	v_sub_u32_e32 v136, v16, v136
	v_and_b32_e32 v136, 0x7fffffc0, v136
	v_mov_b64_e32 v[138:139], s[48:49]
	v_and_b32_e32 v119, 0x3c0, v118
	v_add_u32_e32 v120, 0xffffea00, v136
	v_mad_i64_i32 v[138:139], s[72:73], v135, s11, v[138:139]
	v_or_b32_e32 v112, v120, v6
	v_lshlrev_b32_e32 v136, 2, v119
	v_mov_b32_e32 v137, v3
	v_lshl_add_u64 v[136:137], v[138:139], 0, v[136:137]
	v_mov_b32_e32 v113, v3
	v_or_b32_e32 v138, 4, v112
	v_mov_b32_e32 v139, v3
	v_or_b32_e32 v144, 8, v112
	v_mov_b32_e32 v145, v3
	v_or_b32_e32 v146, 12, v112
	v_mov_b32_e32 v147, v3
	v_or_b32_e32 v68, 16, v112
	v_mov_b32_e32 v69, v3
	v_or_b32_e32 v70, 20, v112
	v_mov_b32_e32 v71, v3
	v_or_b32_e32 v76, 24, v112
	v_mov_b32_e32 v77, v3
	v_or_b32_e32 v78, 28, v112
	v_mov_b32_e32 v79, v3
	v_or_b32_e32 v84, 32, v112
	v_mov_b32_e32 v85, v3
	v_or_b32_e32 v86, 36, v112
	v_mov_b32_e32 v87, v3
	v_or_b32_e32 v92, 40, v112
	v_mov_b32_e32 v93, v3
	v_or_b32_e32 v94, 44, v112
	v_mov_b32_e32 v95, v3
	v_or_b32_e32 v100, 48, v112
	v_mov_b32_e32 v101, v3
	v_or_b32_e32 v102, 52, v112
	v_mov_b32_e32 v103, v3
	v_or_b32_e32 v108, 56, v112
	v_mov_b32_e32 v109, v3
	v_lshl_add_u64 v[114:115], v[136:137], 0, v[2:3]
	v_lshlrev_b64 v[136:137], 12, v[112:113]
	v_lshlrev_b64 v[138:139], 12, v[138:139]
	v_lshlrev_b64 v[144:145], 12, v[144:145]
	v_lshlrev_b64 v[146:147], 12, v[146:147]
	v_lshlrev_b64 v[68:69], 12, v[68:69]
	v_lshlrev_b64 v[70:71], 12, v[70:71]
	v_lshlrev_b64 v[76:77], 12, v[76:77]
	v_lshlrev_b64 v[78:79], 12, v[78:79]
	v_lshlrev_b64 v[84:85], 12, v[84:85]
	v_lshlrev_b64 v[86:87], 12, v[86:87]
	v_lshlrev_b64 v[92:93], 12, v[92:93]
	v_lshlrev_b64 v[94:95], 12, v[94:95]
	v_lshlrev_b64 v[100:101], 12, v[100:101]
	v_lshlrev_b64 v[102:103], 12, v[102:103]
	v_lshlrev_b64 v[108:109], 12, v[108:109]
	v_lshl_add_u64 v[136:137], v[114:115], 0, v[136:137]
	v_lshl_add_u64 v[140:141], v[114:115], 0, v[138:139]
	v_lshl_add_u64 v[144:145], v[114:115], 0, v[144:145]
	v_lshl_add_u64 v[64:65], v[114:115], 0, v[146:147]
	v_lshl_add_u64 v[68:69], v[114:115], 0, v[68:69]
	v_lshl_add_u64 v[72:73], v[114:115], 0, v[70:71]
	v_lshl_add_u64 v[76:77], v[114:115], 0, v[76:77]
	v_lshl_add_u64 v[80:81], v[114:115], 0, v[78:79]
	v_lshl_add_u64 v[84:85], v[114:115], 0, v[84:85]
	v_lshl_add_u64 v[88:89], v[114:115], 0, v[86:87]
	v_lshl_add_u64 v[92:93], v[114:115], 0, v[92:93]
	v_lshl_add_u64 v[96:97], v[114:115], 0, v[94:95]
	v_lshl_add_u64 v[100:101], v[114:115], 0, v[100:101]
	v_lshl_add_u64 v[104:105], v[114:115], 0, v[102:103]
	v_lshl_add_u64 v[108:109], v[114:115], 0, v[108:109]
	v_or_b32_e32 v112, 60, v112
	global_load_dwordx4 v[136:139], v[136:137], off nt
	s_nop 0
	global_load_dwordx4 v[140:143], v[140:141], off nt
	s_nop 0
	global_load_dwordx4 v[144:147], v[144:145], off nt
	s_nop 0
	global_load_dwordx4 v[64:67], v[64:65], off nt
	s_nop 0
	global_load_dwordx4 v[68:71], v[68:69], off nt
	s_nop 0
	global_load_dwordx4 v[72:75], v[72:73], off nt
	s_nop 0
	global_load_dwordx4 v[76:79], v[76:77], off nt
	s_nop 0
	global_load_dwordx4 v[80:83], v[80:81], off nt
	s_nop 0
	global_load_dwordx4 v[84:87], v[84:85], off nt
	s_nop 0
	global_load_dwordx4 v[88:91], v[88:89], off nt
	s_nop 0
	global_load_dwordx4 v[92:95], v[92:93], off nt
	s_nop 0
	global_load_dwordx4 v[96:99], v[96:97], off nt
	s_nop 0
	global_load_dwordx4 v[100:103], v[100:101], off nt
	s_nop 0
	global_load_dwordx4 v[104:107], v[104:105], off nt
	v_lshlrev_b64 v[112:113], 12, v[112:113]
	global_load_dwordx4 v[108:111], v[108:109], off nt
	v_lshl_add_u64 v[112:113], v[114:115], 0, v[112:113]
	global_load_dwordx4 v[112:115], v[112:113], off nt
	v_mul_hi_i32_i24_e32 v117, 0x580000, v135
	v_mul_i32_i24_e32 v116, 0x580000, v135
	v_add_u32_e32 v135, 0x38e0, v20
	s_waitcnt vmcnt(15)
	ds_write2_b32 v20, v136, v137 offset1:1
	ds_write2_b32 v20, v138, v139 offset0:2 offset1:3
	s_waitcnt vmcnt(14)
	ds_write2_b32 v21, v140, v141 offset1:1
	ds_write2_b32 v22, v142, v143 offset1:1
	s_waitcnt vmcnt(13)
	ds_write2_b32 v23, v144, v145 offset1:1
	ds_write2_b32 v24, v146, v147 offset1:1
	s_waitcnt vmcnt(12)
	ds_write2_b32 v25, v64, v65 offset1:1
	ds_write2_b32 v26, v66, v67 offset1:1
	s_waitcnt vmcnt(11)
	ds_write2_b32 v27, v68, v69 offset1:1
	ds_write2_b32 v28, v70, v71 offset1:1
	s_waitcnt vmcnt(10)
	ds_write2_b32 v29, v72, v73 offset1:1
	ds_write2_b32 v30, v74, v75 offset1:1
	s_waitcnt vmcnt(9)
	ds_write2_b32 v31, v76, v77 offset1:1
	ds_write2_b32 v32, v78, v79 offset1:1
	s_waitcnt vmcnt(8)
	ds_write2_b32 v33, v80, v81 offset1:1
	ds_write2_b32 v34, v82, v83 offset1:1
	s_waitcnt vmcnt(7)
	ds_write2_b32 v35, v84, v85 offset1:1
	ds_write2_b32 v36, v86, v87 offset1:1
	s_waitcnt vmcnt(6)
	ds_write2_b32 v37, v88, v89 offset1:1
	ds_write2_b32 v38, v90, v91 offset1:1
	s_waitcnt vmcnt(5)
	ds_write2_b32 v39, v92, v93 offset1:1
	ds_write2_b32 v40, v94, v95 offset1:1
	s_waitcnt vmcnt(4)
	ds_write2_b32 v41, v96, v97 offset1:1
	ds_write2_b32 v42, v98, v99 offset1:1
	s_waitcnt vmcnt(3)
	ds_write2_b32 v43, v100, v101 offset1:1
	ds_write2_b32 v44, v102, v103 offset1:1
	s_waitcnt vmcnt(2)
	ds_write2_b32 v45, v104, v105 offset1:1
	ds_write2_b32 v46, v106, v107 offset1:1
	v_readlane_b32 s72, v250, 8
	s_waitcnt vmcnt(1)
	ds_write2_b32 v135, v108, v109 offset1:1
	v_add_u32_e32 v135, 0x38e8, v20
	ds_write2_b32 v135, v110, v111 offset1:1
	v_add_u32_e32 v135, 0x3cf0, v20
	s_waitcnt vmcnt(0)
	ds_write2_b32 v135, v112, v113 offset1:1
	v_add_u32_e32 v135, 0x3cf8, v20
	ds_write2_b32 v135, v114, v115 offset1:1
	s_waitcnt lgkmcnt(0)
; #define LAS __attribute__((address_space(3)))
; __device__ __forceinline__ unsigned cvt_pk_bf16(float lo, float hi) { const f32x2 v = {lo, hi}; const bf16v2_t r = __builtin_convertvector(v, bf16v2_t); return __builtin_bit_cast(unsigned, r); }
; __device__ __forceinline__ void cvt_item(const float* W, int K, int N, bf16_t* WT, int drow0, int k0, int n0, LAS float* scr, int lane) {
;     ...
;     asm volatile("s_waitcnt lgkmcnt(0)" ::: "memory");
;     const int c = lane & 7;
; #pragma unroll
;     for (int j = 0; j < 8; ++j) { const int n = (lane >> 3) + 8 * j; const LAS float* s = scr + (8 * c) * 65 + n;
;         u32x4 o; o.x = cvt_pk_bf16(s[0 * 65], s[1 * 65]); o.y = cvt_pk_bf16(s[2 * 65], s[3 * 65]); o.z = cvt_pk_bf16(s[4 * 65], s[5 * 65]); o.w = cvt_pk_bf16(s[6 * 65], s[7 * 65]);
;         __builtin_nontemporal_store(o, (u32x4*)(WT + ((size_t)((drow0 + n) >> 7) * (K >> 6) + (k0 >> 6)) * 8192 + ((drow0 + n) & 127) * 64 + 8 * c)); }
;     asm volatile("s_waitcnt lgkmcnt(0)" ::: "memory");
; }
	ds_read2_b32 v[140:141], v8 offset0:65 offset1:73
	ds_read2_b32 v[142:143], v8 offset1:8
	ds_read2_b32 v[144:145], v8 offset0:130 offset1:138
	ds_read2_b32 v[146:147], v8 offset0:195 offset1:203
	v_add_u32_e32 v135, 0x400, v8
	ds_read2_b32 v[64:65], v135 offset0:4 offset1:12
	ds_read2_b32 v[66:67], v135 offset0:69 offset1:77
	ds_read2_b32 v[68:69], v135 offset0:134 offset1:142
	ds_read2_b32 v[70:71], v135 offset0:199 offset1:207
	v_lshrrev_b32_e32 v72, 6, v120
	s_waitcnt lgkmcnt(6)
	v_cvt_pk_bf16_f32 v136, v142, v140
	v_bfe_u32 v142, v118, 7, 3
	v_readlane_b32 s73, v250, 9
	v_or_b32_e32 v140, v119, v7
	v_mad_u32_u24 v72, v142, 44, v72
	v_mov_b32_e32 v73, v3
	v_lshl_add_u64 v[116:117], s[72:73], 0, v[116:117]
	v_lshlrev_b64 v[72:73], 14, v[72:73]
	v_lshlrev_b32_e32 v140, 7, v140
	v_lshl_add_u64 v[72:73], v[116:117], 0, v[72:73]
	v_and_b32_e32 v74, 0x2380, v140
	v_mov_b32_e32 v75, v3
	v_lshl_add_u64 v[74:75], v[72:73], 0, v[74:75]
	v_lshlrev_b32_e32 v76, 1, v130
	v_mov_b32_e32 v77, v3
	v_or_b32_e32 v140, v119, v9
	s_waitcnt lgkmcnt(4)
	v_cvt_pk_bf16_f32 v137, v144, v146
	s_waitcnt lgkmcnt(2)
	v_cvt_pk_bf16_f32 v138, v64, v66
	s_waitcnt lgkmcnt(0)
	v_cvt_pk_bf16_f32 v139, v68, v70
	v_lshl_add_u64 v[74:75], v[74:75], 0, v[76:77]
	v_lshlrev_b32_e32 v140, 7, v140
	global_store_dwordx4 v[74:75], v[136:139], off nt
	v_and_b32_e32 v140, 0x2780, v140
	s_nop 0
	v_cvt_pk_bf16_f32 v136, v143, v141
	v_mov_b32_e32 v141, v3
	v_lshl_add_u64 v[140:141], v[72:73], 0, v[140:141]
	v_cvt_pk_bf16_f32 v137, v145, v147
	v_cvt_pk_bf16_f32 v138, v65, v67
	v_cvt_pk_bf16_f32 v139, v69, v71
	v_lshl_add_u64 v[140:141], v[140:141], 0, v[76:77]
	ds_read2_b32 v[142:143], v8 offset0:16 offset1:24
	ds_read2_b32 v[144:145], v8 offset0:81 offset1:89
	ds_read2_b32 v[146:147], v8 offset0:146 offset1:154
	ds_read2_b32 v[64:65], v8 offset0:211 offset1:219
	ds_read2_b32 v[66:67], v135 offset0:20 offset1:28
	ds_read2_b32 v[68:69], v135 offset0:85 offset1:93
	ds_read2_b32 v[70:71], v135 offset0:150 offset1:158
	ds_read2_b32 v[74:75], v135 offset0:215 offset1:223
	global_store_dwordx4 v[140:141], v[136:139], off nt
	v_or_b32_e32 v140, v119, v10
	v_lshlrev_b32_e32 v140, 7, v140
	v_and_b32_e32 v140, 0x2b80, v140
	v_mov_b32_e32 v141, v3
	v_lshl_add_u64 v[140:141], v[72:73], 0, v[140:141]
	s_waitcnt lgkmcnt(6)
	v_cvt_pk_bf16_f32 v136, v142, v144
	s_waitcnt lgkmcnt(4)
	v_cvt_pk_bf16_f32 v137, v146, v64
	s_waitcnt lgkmcnt(2)
	v_cvt_pk_bf16_f32 v138, v66, v68
	s_waitcnt lgkmcnt(0)
	v_cvt_pk_bf16_f32 v139, v70, v74
	v_lshl_add_u64 v[140:141], v[140:141], 0, v[76:77]
	global_store_dwordx4 v[140:141], v[136:139], off nt
	v_or_b32_e32 v140, v119, v11
	v_lshlrev_b32_e32 v140, 7, v140
	v_and_b32_e32 v140, 0x2f80, v140
	v_mov_b32_e32 v141, v3
	v_lshl_add_u64 v[140:141], v[72:73], 0, v[140:141]
	v_cvt_pk_bf16_f32 v136, v143, v145
	v_cvt_pk_bf16_f32 v137, v147, v65
	v_cvt_pk_bf16_f32 v138, v67, v69
	v_cvt_pk_bf16_f32 v139, v71, v75
	v_lshl_add_u64 v[140:141], v[140:141], 0, v[76:77]
	ds_read2_b32 v[142:143], v8 offset0:32 offset1:40
	ds_read2_b32 v[144:145], v8 offset0:97 offset1:105
	ds_read2_b32 v[146:147], v8 offset0:162 offset1:170
	ds_read2_b32 v[64:65], v8 offset0:227 offset1:235
	ds_read2_b32 v[66:67], v135 offset0:36 offset1:44
	ds_read2_b32 v[68:69], v135 offset0:101 offset1:109
	ds_read2_b32 v[70:71], v135 offset0:166 offset1:174
	ds_read2_b32 v[74:75], v135 offset0:231 offset1:239
	global_store_dwordx4 v[140:141], v[136:139], off nt
	v_or_b32_e32 v140, v119, v12
	v_lshlrev_b32_e32 v140, 7, v140
	v_and_b32_e32 v140, 0x3380, v140
	v_mov_b32_e32 v141, v3
	v_lshl_add_u64 v[140:141], v[72:73], 0, v[140:141]
	s_waitcnt lgkmcnt(6)
	v_cvt_pk_bf16_f32 v136, v142, v144
	s_waitcnt lgkmcnt(4)
	v_cvt_pk_bf16_f32 v137, v146, v64
	s_waitcnt lgkmcnt(2)
	v_cvt_pk_bf16_f32 v138, v66, v68
	s_waitcnt lgkmcnt(0)
	v_cvt_pk_bf16_f32 v139, v70, v74
	v_lshl_add_u64 v[140:141], v[140:141], 0, v[76:77]
	global_store_dwordx4 v[140:141], v[136:139], off nt
	v_or_b32_e32 v140, v119, v13
	v_lshlrev_b32_e32 v140, 7, v140
	v_cvt_pk_bf16_f32 v136, v143, v145
	v_cvt_pk_bf16_f32 v137, v147, v65
	v_cvt_pk_bf16_f32 v138, v67, v69
	v_cvt_pk_bf16_f32 v139, v71, v75
	v_and_b32_e32 v140, 0x3780, v140
	v_mov_b32_e32 v141, v3
	ds_read2_b32 v[142:143], v8 offset0:48 offset1:56
	ds_read2_b32 v[144:145], v8 offset0:113 offset1:121
	ds_read2_b32 v[146:147], v8 offset0:178 offset1:186
	ds_read2_b32 v[64:65], v8 offset0:243 offset1:251
	ds_read2_b32 v[66:67], v135 offset0:52 offset1:60
	ds_read2_b32 v[68:69], v135 offset0:117 offset1:125
	ds_read2_b32 v[70:71], v135 offset0:182 offset1:190
	ds_read2_b32 v[74:75], v135 offset0:247 offset1:255
	v_lshl_add_u64 v[140:141], v[72:73], 0, v[140:141]
	v_or_b32_e32 v135, v119, v14
	v_lshl_add_u64 v[140:141], v[140:141], 0, v[76:77]
	v_lshlrev_b32_e32 v135, 7, v135
	global_store_dwordx4 v[140:141], v[136:139], off nt
	v_and_b32_e32 v140, 0x3b80, v135
	v_mov_b32_e32 v141, v3
	v_lshl_add_u64 v[140:141], v[72:73], 0, v[140:141]
	v_or_b32_e32 v135, v119, v15
	s_waitcnt lgkmcnt(6)
	v_cvt_pk_bf16_f32 v136, v142, v144
	s_waitcnt lgkmcnt(4)
	v_cvt_pk_bf16_f32 v137, v146, v64
	s_waitcnt lgkmcnt(2)
	v_cvt_pk_bf16_f32 v138, v66, v68
	s_waitcnt lgkmcnt(0)
	v_cvt_pk_bf16_f32 v139, v70, v74
	v_lshl_add_u64 v[140:141], v[140:141], 0, v[76:77]
	v_lshlrev_b32_e32 v135, 7, v135
	global_store_dwordx4 v[140:141], v[136:139], off nt
	v_and_b32_e32 v140, 0x3f80, v135
	v_mov_b32_e32 v141, v3
	v_lshl_add_u64 v[140:141], v[72:73], 0, v[140:141]
	v_cvt_pk_bf16_f32 v136, v143, v145
	v_cvt_pk_bf16_f32 v137, v147, v65
	v_cvt_pk_bf16_f32 v138, v67, v69
	v_cvt_pk_bf16_f32 v139, v71, v75
	v_lshl_add_u64 v[140:141], v[140:141], 0, v[76:77]
	global_store_dwordx4 v[140:141], v[136:139], off nt
	s_waitcnt lgkmcnt(0)
; #define LAS __attribute__((address_space(3)))
; __device__ __forceinline__ void cvt_item(const float* W, int K, int N, bf16_t* WT, int drow0, int k0, int n0, LAS float* scr, int lane) {
;     f32x4 v[16];
;     const int lr = lane >> 4, lc4 = (lane & 15) * 4;
; #pragma unroll
;     for (int i = 0; i < 16; ++i) v[i] = __builtin_nontemporal_load((const f32x4*)(W + (size_t)(k0 + 4 * i + lr) * N + n0 + lc4));
; #pragma unroll
;     for (int i = 0; i < 16; ++i) { LAS float* d = scr + (4 * i + lr) * 65 + lc4; d[0] = v[i][0]; d[1] = v[i][1]; d[2] = v[i][2]; d[3] = v[i][3]; }
; __device__ __forceinline__ void phase_cvt_moe(LAS unsigned char* lds, const CvtMoe a) {
;     ...
;         if (r < 2 * IG) { const int up = r / IG; r %= IG; const int nblk = FF / 64, kb = r / nblk, nb = r % nblk, n0 = nb * 64;
;             cvt_item((up ? a.wu : a.wg) + (size_t)e * D * FF, D, FF, a.gu + (size_t)e * 2 * FF * D, (n0 / 128) * 256 + up * 128 + (n0 % 128), kb * 64, n0, scr, lane); }
.Lcvp4b_60:
	s_andn2_saveexec_b64 s[8:9], s[8:9]
	s_cbranch_execz .Lcvp4b_57
	v_mul_i32_i24_e32 v137, 0xba3, v136
	v_lshrrev_b32_e32 v138, 31, v137
	v_ashrrev_i32_e32 v137, 21, v137
	v_add_u16_e32 v117, v137, v138
	v_mul_lo_u16_e32 v137, 0x2c0, v117
	v_sub_u16_e32 v137, v136, v137
	v_mul_i32_i24_sdwa v138, sext(v137), s64 dst_sel:DWORD dst_unused:UNUSED_PAD src0_sel:WORD_0 src1_sel:DWORD
	v_lshrrev_b32_e32 v139, 31, v138
	v_ashrrev_i32_e32 v138, 17, v138
	v_add_u16_e32 v138, v138, v139
	v_bfe_i32 v116, v138, 0, 16
	v_mul_lo_u16_e32 v138, 44, v138
	v_add_u32_e32 v136, 0x2bf, v136
	v_sub_u16_e32 v122, v137, v138
	v_mov_b32_e32 v137, s41
	v_mov_b32_e32 v138, s39
	v_cmp_gt_u32_e32 vcc, s10, v136
	v_mov_b32_e32 v136, s40
	v_lshlrev_b32_sdwa v118, v47, sext(v122) dst_sel:DWORD dst_unused:UNUSED_PAD src0_sel:DWORD src1_sel:WORD_0
	v_cndmask_b32_e32 v137, v137, v138, vcc
	v_mov_b32_e32 v138, s38
	v_cndmask_b32_e32 v136, v136, v138, vcc
	v_mad_i64_i32 v[136:137], s[72:73], v135, s11, v[136:137]
	v_lshl_or_b32 v138, v116, 6, v6
	v_ashrrev_i32_e32 v119, 31, v118
	v_lshl_add_u64 v[136:137], v[118:119], 2, v[136:137]
	v_mul_i32_i24_e32 v138, 0xb00, v138
	v_lshl_add_u64 v[136:137], v[136:137], 0, v[2:3]
	v_ashrrev_i32_e32 v139, 31, v138
	v_lshl_add_u64 v[112:113], v[138:139], 2, v[136:137]
	v_add_co_u32_e32 v140, vcc, s65, v112
	v_readlane_b32 s72, v250, 6
	s_nop 0
	v_addc_co_u32_e32 v141, vcc, 0, v113, vcc
	v_add_co_u32_e32 v144, vcc, s66, v112
	global_load_dwordx4 v[136:139], v[112:113], off nt
	s_nop 0
	global_load_dwordx4 v[140:143], v[140:141], off nt
	v_addc_co_u32_e32 v145, vcc, 0, v113, vcc
	v_add_co_u32_e32 v64, vcc, s67, v112
	v_readlane_b32 s73, v250, 7
	s_nop 0
	v_addc_co_u32_e32 v65, vcc, 0, v113, vcc
	v_add_co_u32_e32 v68, vcc, s16, v112
	global_load_dwordx4 v[144:147], v[144:145], off nt
	s_nop 0
	global_load_dwordx4 v[64:67], v[64:65], off nt
	v_addc_co_u32_e32 v69, vcc, 0, v113, vcc
	v_add_co_u32_e32 v72, vcc, s68, v112
	v_mov_b64_e32 v[120:121], s[72:73]
	s_nop 0
	v_addc_co_u32_e32 v73, vcc, 0, v113, vcc
	v_add_co_u32_e32 v76, vcc, s69, v112
	global_load_dwordx4 v[68:71], v[68:69], off nt
	s_nop 0
	global_load_dwordx4 v[72:75], v[72:73], off nt
	v_addc_co_u32_e32 v77, vcc, 0, v113, vcc
	v_add_co_u32_e32 v80, vcc, s19, v112
	v_ashrrev_i16_e32 v119, 15, v118
	s_nop 0
	v_addc_co_u32_e32 v81, vcc, 0, v113, vcc
	v_add_co_u32_e32 v84, vcc, s20, v112
	global_load_dwordx4 v[76:79], v[76:77], off nt
	s_nop 0
	global_load_dwordx4 v[80:83], v[80:81], off nt
	v_addc_co_u32_e32 v85, vcc, 0, v113, vcc
	v_add_co_u32_e32 v88, vcc, s21, v112
	v_mad_i64_i32 v[120:121], s[72:73], v135, s11, v[120:121]
	s_nop 0
	v_addc_co_u32_e32 v89, vcc, 0, v113, vcc
	v_add_co_u32_e32 v92, vcc, s70, v112
	global_load_dwordx4 v[84:87], v[84:85], off nt
	s_nop 0
	global_load_dwordx4 v[88:91], v[88:89], off nt
	v_addc_co_u32_e32 v93, vcc, 0, v113, vcc
	v_add_co_u32_e32 v96, vcc, s23, v112
	v_lshrrev_b16_e32 v135, 7, v122
	s_nop 0
	v_addc_co_u32_e32 v97, vcc, 0, v113, vcc
	v_add_co_u32_e32 v100, vcc, s24, v112
	global_load_dwordx4 v[92:95], v[92:93], off nt
	s_nop 0
	global_load_dwordx4 v[96:99], v[96:97], off nt
	v_addc_co_u32_e32 v101, vcc, 0, v113, vcc
	v_add_co_u32_e32 v104, vcc, s25, v112
	v_lshrrev_b16_e32 v119, 9, v119
	s_nop 0
	v_addc_co_u32_e32 v105, vcc, 0, v113, vcc
	v_add_co_u32_e32 v108, vcc, s26, v112
	global_load_dwordx4 v[100:103], v[100:101], off nt
	s_nop 0
	global_load_dwordx4 v[104:107], v[104:105], off nt
	v_addc_co_u32_e32 v109, vcc, 0, v113, vcc
	global_load_dwordx4 v[108:111], v[108:109], off nt
	v_add_co_u32_e32 v112, vcc, s27, v112
	v_and_b32_e32 v135, 1, v135
	s_nop 0
	v_addc_co_u32_e32 v113, vcc, 0, v113, vcc
	global_load_dwordx4 v[112:115], v[112:113], off nt
	v_add_u16_e32 v119, v118, v119
	v_add_u16_e32 v135, v122, v135
	v_and_b32_e32 v119, 0xffffff80, v119
	v_ashrrev_i16_sdwa v135, v132, sext(v135) dst_sel:DWORD dst_unused:UNUSED_PAD src0_sel:DWORD src1_sel:BYTE_0
	v_sub_u16_e32 v118, v118, v119
	v_lshlrev_b32_sdwa v135, v133, sext(v135) dst_sel:DWORD dst_unused:UNUSED_PAD src0_sel:DWORD src1_sel:WORD_0
	v_lshlrev_b32_sdwa v117, v134, sext(v117) dst_sel:DWORD dst_unused:UNUSED_PAD src0_sel:DWORD src1_sel:WORD_0
	v_bfe_i32 v118, v118, 0, 16
	v_add3_u32 v135, v135, v117, v118
	v_ashrrev_i32_e32 v117, 31, v116
	s_waitcnt vmcnt(15)
	ds_write2_b32 v20, v136, v137 offset1:1
	ds_write2_b32 v20, v138, v139 offset0:2 offset1:3
	s_waitcnt vmcnt(14)
	ds_write2_b32 v21, v140, v141 offset1:1
	ds_write2_b32 v22, v142, v143 offset1:1
	s_waitcnt vmcnt(13)
	ds_write2_b32 v23, v144, v145 offset1:1
	ds_write2_b32 v24, v146, v147 offset1:1
	s_waitcnt vmcnt(12)
	ds_write2_b32 v25, v64, v65 offset1:1
	ds_write2_b32 v26, v66, v67 offset1:1
	s_waitcnt vmcnt(11)
	ds_write2_b32 v27, v68, v69 offset1:1
	ds_write2_b32 v28, v70, v71 offset1:1
	s_waitcnt vmcnt(10)
	ds_write2_b32 v29, v72, v73 offset1:1
	ds_write2_b32 v30, v74, v75 offset1:1
	s_waitcnt vmcnt(9)
	ds_write2_b32 v31, v76, v77 offset1:1
	ds_write2_b32 v32, v78, v79 offset1:1
	s_waitcnt vmcnt(8)
	ds_write2_b32 v33, v80, v81 offset1:1
	ds_write2_b32 v34, v82, v83 offset1:1
	s_waitcnt vmcnt(7)
	ds_write2_b32 v35, v84, v85 offset1:1
	ds_write2_b32 v36, v86, v87 offset1:1
	s_waitcnt vmcnt(6)
	ds_write2_b32 v37, v88, v89 offset1:1
	ds_write2_b32 v38, v90, v91 offset1:1
	s_waitcnt vmcnt(5)
	ds_write2_b32 v39, v92, v93 offset1:1
	ds_write2_b32 v40, v94, v95 offset1:1
	s_waitcnt vmcnt(4)
	ds_write2_b32 v41, v96, v97 offset1:1
	ds_write2_b32 v42, v98, v99 offset1:1
	s_waitcnt vmcnt(3)
	ds_write2_b32 v43, v100, v101 offset1:1
	ds_write2_b32 v44, v102, v103 offset1:1
	s_waitcnt vmcnt(2)
; #define LAS __attribute__((address_space(3)))
; __device__ __forceinline__ unsigned cvt_pk_bf16(float lo, float hi) { const f32x2 v = {lo, hi}; const bf16v2_t r = __builtin_convertvector(v, bf16v2_t); return __builtin_bit_cast(unsigned, r); }
; __device__ __forceinline__ void cvt_item(const float* W, int K, int N, bf16_t* WT, int drow0, int k0, int n0, LAS float* scr, int lane) {
;     ...
;     for (int i = 0; i < 16; ++i) { LAS float* d = scr + (4 * i + lr) * 65 + lc4; d[0] = v[i][0]; d[1] = v[i][1]; d[2] = v[i][2]; d[3] = v[i][3]; }
;     asm volatile("s_waitcnt lgkmcnt(0)" ::: "memory");
;     const int c = lane & 7;
; #pragma unroll
;     for (int j = 0; j < 8; ++j) { const int n = (lane >> 3) + 8 * j; const LAS float* s = scr + (8 * c) * 65 + n;
;         u32x4 o; o.x = cvt_pk_bf16(s[0 * 65], s[1 * 65]); o.y = cvt_pk_bf16(s[2 * 65], s[3 * 65]); o.z = cvt_pk_bf16(s[4 * 65], s[5 * 65]); o.w = cvt_pk_bf16(s[6 * 65], s[7 * 65]);
;         __builtin_nontemporal_store(o, (u32x4*)(WT + ((size_t)((drow0 + n) >> 7) * (K >> 6) + (k0 >> 6)) * 8192 + ((drow0 + n) & 127) * 64 + 8 * c)); }
;     asm volatile("s_waitcnt lgkmcnt(0)" ::: "memory");
; }
; __device__ __forceinline__ void phase_cvt_moe(LAS unsigned char* lds, const CvtMoe a) {
;     ...
;     for (int it = gw; it < 2 * NE * (2 * IG + ID); it += NGW) {
	ds_write2_b32 v45, v104, v105 offset1:1
	ds_write2_b32 v46, v106, v107 offset1:1
	v_add_u32_e32 v136, 0x38e0, v20
	v_add_u32_e32 v78, 0x400, v8
	s_waitcnt vmcnt(1)
	ds_write2_b32 v136, v108, v109 offset1:1
	v_add_u32_e32 v136, 0x38e8, v20
	ds_write2_b32 v136, v110, v111 offset1:1
	v_add_u32_e32 v136, 0x3cf0, v20
	v_ashrrev_i32_e32 v72, 7, v135
	v_ashrrev_i32_e32 v73, 31, v72
	s_waitcnt vmcnt(0)
	ds_write2_b32 v136, v112, v113 offset1:1
	v_add_u32_e32 v136, 0x3cf8, v20
	ds_write2_b32 v136, v114, v115 offset1:1
	s_waitcnt lgkmcnt(0)
	ds_read2_b32 v[140:141], v8 offset0:65 offset1:73
	ds_read2_b32 v[142:143], v8 offset1:8
	ds_read2_b32 v[144:145], v8 offset0:130 offset1:138
	ds_read2_b32 v[146:147], v8 offset0:195 offset1:203
	ds_read2_b32 v[64:65], v78 offset0:4 offset1:12
	ds_read2_b32 v[66:67], v78 offset0:69 offset1:77
	ds_read2_b32 v[68:69], v78 offset0:134 offset1:142
	ds_read2_b32 v[70:71], v78 offset0:199 offset1:207
	v_lshlrev_b64 v[72:73], 18, v[72:73]
	s_waitcnt lgkmcnt(6)
	v_cvt_pk_bf16_f32 v136, v142, v140
	v_or_b32_e32 v140, v135, v7
	v_lshlrev_b64 v[74:75], 14, v[116:117]
	v_lshl_add_u64 v[72:73], v[120:121], 0, v[72:73]
	v_lshlrev_b32_e32 v140, 7, v140
	v_lshl_add_u64 v[72:73], v[72:73], 0, v[74:75]
	v_and_b32_e32 v74, 0x3f80, v140
	v_mov_b32_e32 v75, v3
	v_lshl_add_u64 v[74:75], v[72:73], 0, v[74:75]
	v_lshlrev_b32_e32 v76, 1, v130
	v_mov_b32_e32 v77, v3
	v_or_b32_e32 v140, v135, v9
	s_waitcnt lgkmcnt(4)
	v_cvt_pk_bf16_f32 v137, v144, v146
	s_waitcnt lgkmcnt(2)
	v_cvt_pk_bf16_f32 v138, v64, v66
	s_waitcnt lgkmcnt(0)
	v_cvt_pk_bf16_f32 v139, v68, v70
	v_lshl_add_u64 v[74:75], v[74:75], 0, v[76:77]
	v_lshlrev_b32_e32 v140, 7, v140
	global_store_dwordx4 v[74:75], v[136:139], off nt
	v_and_b32_e32 v140, 0x3f80, v140
	s_nop 0
	v_cvt_pk_bf16_f32 v136, v143, v141
	v_mov_b32_e32 v141, v3
	v_lshl_add_u64 v[140:141], v[72:73], 0, v[140:141]
	v_cvt_pk_bf16_f32 v137, v145, v147
	v_cvt_pk_bf16_f32 v138, v65, v67
	v_cvt_pk_bf16_f32 v139, v69, v71
	v_lshl_add_u64 v[140:141], v[140:141], 0, v[76:77]
	ds_read2_b32 v[142:143], v8 offset0:16 offset1:24
	ds_read2_b32 v[144:145], v8 offset0:81 offset1:89
	ds_read2_b32 v[146:147], v8 offset0:146 offset1:154
	ds_read2_b32 v[64:65], v8 offset0:211 offset1:219
	ds_read2_b32 v[66:67], v78 offset0:20 offset1:28
	ds_read2_b32 v[68:69], v78 offset0:85 offset1:93
	ds_read2_b32 v[70:71], v78 offset0:150 offset1:158
	ds_read2_b32 v[74:75], v78 offset0:215 offset1:223
	global_store_dwordx4 v[140:141], v[136:139], off nt
	v_or_b32_e32 v140, v135, v10
	v_lshlrev_b32_e32 v140, 7, v140
	v_and_b32_e32 v140, 0x3f80, v140
	v_mov_b32_e32 v141, v3
	v_lshl_add_u64 v[140:141], v[72:73], 0, v[140:141]
	s_waitcnt lgkmcnt(6)
	v_cvt_pk_bf16_f32 v136, v142, v144
	s_waitcnt lgkmcnt(4)
	v_cvt_pk_bf16_f32 v137, v146, v64
	s_waitcnt lgkmcnt(2)
	v_cvt_pk_bf16_f32 v138, v66, v68
	s_waitcnt lgkmcnt(0)
	v_cvt_pk_bf16_f32 v139, v70, v74
	v_lshl_add_u64 v[140:141], v[140:141], 0, v[76:77]
	global_store_dwordx4 v[140:141], v[136:139], off nt
	v_or_b32_e32 v140, v135, v11
	v_lshlrev_b32_e32 v140, 7, v140
	v_and_b32_e32 v140, 0x3f80, v140
	v_mov_b32_e32 v141, v3
	v_lshl_add_u64 v[140:141], v[72:73], 0, v[140:141]
	v_cvt_pk_bf16_f32 v136, v143, v145
	v_cvt_pk_bf16_f32 v137, v147, v65
	v_cvt_pk_bf16_f32 v138, v67, v69
	v_cvt_pk_bf16_f32 v139, v71, v75
	v_lshl_add_u64 v[140:141], v[140:141], 0, v[76:77]
	ds_read2_b32 v[142:143], v8 offset0:32 offset1:40
	ds_read2_b32 v[144:145], v8 offset0:97 offset1:105
	ds_read2_b32 v[146:147], v8 offset0:162 offset1:170
	ds_read2_b32 v[64:65], v8 offset0:227 offset1:235
	ds_read2_b32 v[66:67], v78 offset0:36 offset1:44
	ds_read2_b32 v[68:69], v78 offset0:101 offset1:109
	ds_read2_b32 v[70:71], v78 offset0:166 offset1:174
	ds_read2_b32 v[74:75], v78 offset0:231 offset1:239
	global_store_dwordx4 v[140:141], v[136:139], off nt
	v_or_b32_e32 v140, v135, v12
	v_lshlrev_b32_e32 v140, 7, v140
	v_and_b32_e32 v140, 0x3f80, v140
	v_mov_b32_e32 v141, v3
	v_lshl_add_u64 v[140:141], v[72:73], 0, v[140:141]
	s_waitcnt lgkmcnt(6)
	v_cvt_pk_bf16_f32 v136, v142, v144
	s_waitcnt lgkmcnt(4)
	v_cvt_pk_bf16_f32 v137, v146, v64
	s_waitcnt lgkmcnt(2)
	v_cvt_pk_bf16_f32 v138, v66, v68
	s_waitcnt lgkmcnt(0)
	v_cvt_pk_bf16_f32 v139, v70, v74
	v_lshl_add_u64 v[140:141], v[140:141], 0, v[76:77]
	global_store_dwordx4 v[140:141], v[136:139], off nt
	v_or_b32_e32 v140, v135, v13
	v_lshlrev_b32_e32 v140, 7, v140
	v_and_b32_e32 v140, 0x3f80, v140
	v_mov_b32_e32 v141, v3
	v_lshl_add_u64 v[140:141], v[72:73], 0, v[140:141]
	v_cvt_pk_bf16_f32 v136, v143, v145
	v_cvt_pk_bf16_f32 v137, v147, v65
	v_cvt_pk_bf16_f32 v138, v67, v69
	v_cvt_pk_bf16_f32 v139, v71, v75
	v_lshl_add_u64 v[140:141], v[140:141], 0, v[76:77]
	ds_read2_b32 v[142:143], v8 offset0:48 offset1:56
	ds_read2_b32 v[144:145], v8 offset0:113 offset1:121
	ds_read2_b32 v[146:147], v8 offset0:178 offset1:186
	ds_read2_b32 v[64:65], v8 offset0:243 offset1:251
	ds_read2_b32 v[66:67], v78 offset0:52 offset1:60
	ds_read2_b32 v[68:69], v78 offset0:117 offset1:125
	ds_read2_b32 v[70:71], v78 offset0:182 offset1:190
	ds_read2_b32 v[74:75], v78 offset0:247 offset1:255
	global_store_dwordx4 v[140:141], v[136:139], off nt
	v_or_b32_e32 v140, v135, v14
	v_lshlrev_b32_e32 v140, 7, v140
	v_and_b32_e32 v140, 0x3f80, v140
	v_mov_b32_e32 v141, v3
	v_lshl_add_u64 v[140:141], v[72:73], 0, v[140:141]
	v_or_b32_e32 v135, v135, v15
	s_waitcnt lgkmcnt(6)
	v_cvt_pk_bf16_f32 v136, v142, v144
	s_waitcnt lgkmcnt(4)
	v_cvt_pk_bf16_f32 v137, v146, v64
	s_waitcnt lgkmcnt(2)
	v_cvt_pk_bf16_f32 v138, v66, v68
	s_waitcnt lgkmcnt(0)
	v_cvt_pk_bf16_f32 v139, v70, v74
	v_lshl_add_u64 v[140:141], v[140:141], 0, v[76:77]
	v_lshlrev_b32_e32 v135, 7, v135
	global_store_dwordx4 v[140:141], v[136:139], off nt
	v_and_b32_e32 v140, 0x3f80, v135
	v_mov_b32_e32 v141, v3
	v_lshl_add_u64 v[140:141], v[72:73], 0, v[140:141]
	v_cvt_pk_bf16_f32 v136, v143, v145
	v_cvt_pk_bf16_f32 v137, v147, v65
	v_cvt_pk_bf16_f32 v138, v67, v69
	v_cvt_pk_bf16_f32 v139, v71, v75
	v_lshl_add_u64 v[140:141], v[140:141], 0, v[76:77]
	global_store_dwordx4 v[140:141], v[136:139], off nt
	s_waitcnt lgkmcnt(0)
	s_branch .Lcvp4b_57
.Lcvp4b_62:
	s_or_b64 exec, exec, s[4:5]
	s_branch .LBB0_643
